# MoE gate/up GEMM: per-unit pipeline drain (vmcnt(0) behind the gather-index loads) removed, indices consumed after the first counted wait; P21 gain vectors hoisted out of the row loop
# speedup vs baseline: 1.0274x; 1.0077x over previous
; #define PG8_GOFF(dst, pmv) do { if (GATHER) { _Pragma("unroll") for (int _h = 0; _h < 2; ++_h) _Pragma("unroll") for (int _i = 0; _i < 2; ++_i) \
;         dst[_h][_i] = ((unsigned)src[(pmv) * BM + _h * HALF + stR[_i]] * (unsigned)K + (unsigned)stC[_i]) * 2u; } } while (0)
; #define PG8_GOFF(dst, pmv) do { if (GATHER) { _Pragma("unroll") for (int _h = 0; _h < 2; ++_h) _Pragma("unroll") for (int _i = 0; _i < 2; ++_i) { int _R, _C; stage_rc(tid * 16 + _i * 8192, _R, _C); \
;         dst[_h][_i] = ((unsigned)src[(pmv) * BM + _h * HALF + _R] * (unsigned)K + (unsigned)_C) * 2u; } } } while (0)
; template <class Epi, class Sched, bool GATHER = false>
; __device__ __forceinline__ void gemm_phase(LAS unsigned char* lds, const Gemm g, const Sched& S, const Epi& E, const int* src = nullptr) {
;     ...
;         const bool has_next = S.next(ui + 1, nxt);
;         const size_t nHA = has_next ? (nxt.hf ? (size_t)0 : hstepA) : cHA;
;         const char* nA = (has_next && !GATHER) ? PG8_ABASE(nxt) : cA; const char* nB = has_next ? (const char*)g.Bt + (size_t)nxt.pn * tstep : cB;
;         if (GATHER) { if (has_next) PG8_GOFF(voffN, nxt.pm); else {
; #pragma unroll
;             for (int _h = 0; _h < 2; ++_h)
; #pragma unroll
;                 for (int _i = 0; _i < 2; ++_i) voffN[_h][_i] = voffA[_h][_i]; } }
.LBB0_827:
	s_andn2_b64 vcc, exec, s[4:5]
	s_mov_b64 s[64:65], s[4:5]
	v_mov_b32_e32 v230, v210
	v_mov_b32_e32 v231, v208
	v_mov_b32_e32 v232, v206
	v_mov_b32_e32 v233, v234
	s_cbranch_vccnz .LBB0_829
	s_lshl_b32 s6, s44, 8
	v_or_b32_e32 v4, s6, v1
	v_readlane_b32 s8, v255, 12
	v_or_b32_e32 v8, s6, v220
	s_bitset1_b32 s6, 7
	v_ashrrev_i32_e32 v5, 31, v4
	v_readlane_b32 s9, v255, 13
	v_or_b32_e32 v10, s6, v1
	v_or_b32_e32 v12, s6, v220
	v_lshl_add_u64 v[4:5], v[4:5], 2, s[8:9]
	v_ashrrev_i32_e32 v9, 31, v8
	v_ashrrev_i32_e32 v11, 31, v10
	v_ashrrev_i32_e32 v13, 31, v12
	v_lshl_add_u64 v[8:9], v[8:9], 2, s[8:9]
	v_lshl_add_u64 v[10:11], v[10:11], 2, s[8:9]
	v_lshl_add_u64 v[12:13], v[12:13], 2, s[8:9]
	global_load_dword v236, v[4:5], off
	s_nop 0
	global_load_dword v237, v[8:9], off
	global_load_dword v238, v[10:11], off
	global_load_dword v239, v[12:13], off
	s_nop 0
	s_nop 0
	s_nop 0
	s_nop 0
	s_nop 0

; #define PG8_STAGE(bufoff, gbase, voff) do { _Pragma("unroll") for (int _i = 0; _i < 2; ++_i) \
;         __builtin_amdgcn_global_load_lds((const unsigned*)((const char*)(gbase) + (voff)[_i]), (LAS unsigned*)(lds + (bufoff) + ldsw + _i * 8192), 16, 0, 0); } while (0)
; #define PG8_LDA(dst, b, h) do { _Pragma("unroll") for (int m = 0; m < 4; ++m) _Pragma("unroll") for (int k = 0; k < 2; ++k) dst[m][k] = *(const LAS bf16x8*)(lds + PG8_SA(b, h) + aoff + m * 2048 + k * 1024); } while (0)
; #define PG8_LDB(dst, b, h) do { _Pragma("unroll") for (int n = 0; n < 2; ++n) _Pragma("unroll") for (int k = 0; k < 2; ++k) dst[n][k] = *(const LAS bf16x8*)(lds + PG8_SB(b, h) + boff + n * 2048 + k * 1024); } while (0)
; #define PG8_MMA(ai, bj, At, Bt) do { __builtin_amdgcn_s_setprio(1); _Pragma("unroll") for (int m = 0; m < 4; ++m) _Pragma("unroll") for (int n = 0; n < 2; ++n) _Pragma("unroll") for (int k = 0; k < 2; ++k) \
;         acc[ai][bj][m][n] = __builtin_amdgcn_mfma_f32_16x16x32_bf16(Bt[n][k], At[m][k], acc[ai][bj][m][n], 0, 0, 0); __builtin_amdgcn_s_setprio(0); } while (0)
; #define PG8_WAIT_V(n) asm volatile("s_waitcnt vmcnt(" #n ")" ::: "memory")
; #define PG8_WAIT_L(n) asm volatile("s_waitcnt lgkmcnt(" #n ")" ::: "memory")
; #define PG8_BAR __builtin_amdgcn_s_barrier()
; #define PG8_SCHED __builtin_amdgcn_sched_barrier(0)
; #define PG8_STAGE(bufoff, gbase, voff) do { _Pragma("unroll") for (int _i = 0; _i < 2; ++_i) \
;         __builtin_amdgcn_global_load_lds((const unsigned*)((const char*)(gbase) + (voff)[_i]), (LAS unsigned*)(lds + (bufoff) + ldsw + _i * 8192), 16, 0, 0); } while (0)
; #define PG8_WAIT_V(n) asm volatile("s_waitcnt vmcnt(" #n ")" ::: "memory")
; #define PG8_BAR __builtin_amdgcn_s_barrier()
; template <class Epi, class Sched, bool GATHER = false>
; __device__ __forceinline__ void gemm_phase(LAS unsigned char* lds, const Gemm g, const Sched& S, const Epi& E, const int* src = nullptr) {
;     ...
;             PG8_LDB(B1, 0, 1); PG8_STAGE(PG8_SB(0, 0), b2, voffB);
;             PG8_BAR; PG8_WAIT_L(0); PG8_MMA(0, 1, At, B1); PG8_BAR;
;             if (full) PG8_LDA(At, 0, 1); PG8_STAGE(PG8_SA(0, 0), a2, va2[0]);
;             PG8_BAR; PG8_WAIT_L(0); if (full) PG8_MMA(1, 0, At, B0); PG8_BAR; PG8_SCHED;
;             PG8_STAGE(PG8_SB(0, 1), b2 + hstep, voffB);
;             PG8_WAIT_V(6); PG8_BAR; if (full) PG8_MMA(1, 1, At, B1); PG8_BAR;
.LBB0_835:
	s_barrier
	s_add_u32 s50, s20, 0x80000
	s_addc_u32 s51, s21, 0
	s_mov_b32 m0, s30
	v_lshl_add_u64 v[182:183], s[50:51], 0, v[198:199]
	global_load_lds_dwordx4 v[182:183], off
	v_lshl_add_u64 v[182:183], s[50:51], 0, v[200:201]
	s_mov_b32 m0, s31
	s_and_b64 vcc, exec, s[6:7]
	global_load_lds_dwordx4 v[182:183], off
	s_waitcnt vmcnt(6)
	v_lshl_or_b32 v240, v236, 12, v221
	v_lshl_or_b32 v241, v237, 12, v221
	v_lshl_or_b32 v242, v238, 12, v221
	v_lshl_or_b32 v243, v239, 12, v221
	v_cndmask_b32_e64 v233, v233, v240, s[64:65]
	v_cndmask_b32_e64 v232, v232, v241, s[64:65]
	v_cndmask_b32_e64 v231, v231, v242, s[64:65]
	v_cndmask_b32_e64 v230, v230, v243, s[64:65]
	s_barrier
	s_cbranch_vccnz .LBB0_837
	s_setprio 1
	s_waitcnt lgkmcnt(0)
	v_mfma_f32_16x16x32_bf16 v[62:65], v[166:169], v[146:149], v[62:65]
	v_mfma_f32_16x16x32_bf16 v[54:57], v[174:177], v[146:149], v[54:57]
	v_mfma_f32_16x16x32_bf16 v[46:49], v[166:169], v[142:145], v[46:49]
	v_mfma_f32_16x16x32_bf16 v[38:41], v[174:177], v[142:145], v[38:41]
	v_mfma_f32_16x16x32_bf16 v[30:33], v[166:169], v[138:141], v[30:33]
	v_mfma_f32_16x16x32_bf16 v[22:25], v[174:177], v[138:141], v[22:25]
	v_mfma_f32_16x16x32_bf16 v[14:17], v[166:169], v[134:137], v[14:17]
	v_mfma_f32_16x16x32_bf16 v[6:9], v[174:177], v[134:137], v[6:9]
	v_mfma_f32_16x16x32_bf16 v[62:65], v[170:173], v[162:165], v[62:65]
	v_mfma_f32_16x16x32_bf16 v[54:57], v[178:181], v[162:165], v[54:57]
	v_mfma_f32_16x16x32_bf16 v[46:49], v[170:173], v[158:161], v[46:49]
	v_mfma_f32_16x16x32_bf16 v[38:41], v[178:181], v[158:161], v[38:41]
	v_mfma_f32_16x16x32_bf16 v[30:33], v[170:173], v[154:157], v[30:33]
	v_mfma_f32_16x16x32_bf16 v[22:25], v[178:181], v[154:157], v[22:25]
	v_mfma_f32_16x16x32_bf16 v[14:17], v[170:173], v[150:153], v[14:17]
	v_mfma_f32_16x16x32_bf16 v[6:9], v[178:181], v[150:153], v[6:9]
	s_setprio 0

; #define PG8_GOFF(dst, pmv) do { if (GATHER) { _Pragma("unroll") for (int _h = 0; _h < 2; ++_h) _Pragma("unroll") for (int _i = 0; _i < 2; ++_i) \
;         dst[_h][_i] = ((unsigned)src[(pmv) * BM + _h * HALF + stR[_i]] * (unsigned)K + (unsigned)stC[_i]) * 2u; } } while (0)
; #define PG8_GOFF(dst, pmv) do { if (GATHER) { _Pragma("unroll") for (int _h = 0; _h < 2; ++_h) _Pragma("unroll") for (int _i = 0; _i < 2; ++_i) { int _R, _C; stage_rc(tid * 16 + _i * 8192, _R, _C); \
;         dst[_h][_i] = ((unsigned)src[(pmv) * BM + _h * HALF + _R] * (unsigned)K + (unsigned)_C) * 2u; } } } while (0)
; template <class Epi, class Sched, bool GATHER = false>
; __device__ __forceinline__ void gemm_phase(LAS unsigned char* lds, const Gemm g, const Sched& S, const Epi& E, const int* src = nullptr) {
;     ...
;         const bool has_next = S.next(ui + 1, nxt);
;         const size_t nHA = has_next ? (nxt.hf ? (size_t)0 : hstepA) : cHA;
;         const char* nA = (has_next && !GATHER) ? PG8_ABASE(nxt) : cA; const char* nB = has_next ? (const char*)g.Bt + (size_t)nxt.pn * tstep : cB;
;         if (GATHER) { if (has_next) PG8_GOFF(voffN, nxt.pm); else {
; #pragma unroll
;             for (int _h = 0; _h < 2; ++_h)
; #pragma unroll
;                 for (int _i = 0; _i < 2; ++_i) voffN[_h][_i] = voffA[_h][_i]; } }
.LBB0_1709:
	s_andn2_b64 vcc, exec, s[4:5]
	s_mov_b64 s[64:65], s[4:5]
	v_mov_b32_e32 v158, v144
	v_mov_b32_e32 v159, v142
	v_mov_b32_e32 v160, v140
	v_mov_b32_e32 v161, v141
	s_cbranch_vccnz .LBB0_1711
	s_lshl_b32 s11, s39, 8
	v_or_b32_e32 v2, s11, v1
	v_readlane_b32 s12, v255, 12
	v_or_b32_e32 v4, s11, v150
	s_bitset1_b32 s11, 7
	v_ashrrev_i32_e32 v3, 31, v2
	v_readlane_b32 s13, v255, 13
	v_ashrrev_i32_e32 v5, 31, v4
	v_or_b32_e32 v6, s11, v1
	v_or_b32_e32 v8, s11, v150
	v_lshl_add_u64 v[2:3], v[2:3], 2, s[12:13]
	v_lshl_add_u64 v[4:5], v[4:5], 2, s[12:13]
	v_ashrrev_i32_e32 v7, 31, v6
	v_ashrrev_i32_e32 v9, 31, v8
	v_lshl_add_u64 v[6:7], v[6:7], 2, s[12:13]
	v_lshl_add_u64 v[8:9], v[8:9], 2, s[12:13]
	global_load_dword v236, v[2:3], off
	s_nop 0
	global_load_dword v237, v[4:5], off
	s_nop 0
	global_load_dword v238, v[6:7], off
	global_load_dword v239, v[8:9], off
	s_nop 0
	s_nop 0
	s_nop 0
	s_nop 0
	s_nop 0

; #define PG8_STAGE(bufoff, gbase, voff) do { _Pragma("unroll") for (int _i = 0; _i < 2; ++_i) \
;         __builtin_amdgcn_global_load_lds((const unsigned*)((const char*)(gbase) + (voff)[_i]), (LAS unsigned*)(lds + (bufoff) + ldsw + _i * 8192), 16, 0, 0); } while (0)
; #define PG8_LDA(dst, b, h) do { _Pragma("unroll") for (int m = 0; m < 4; ++m) _Pragma("unroll") for (int k = 0; k < 2; ++k) dst[m][k] = *(const LAS bf16x8*)(lds + PG8_SA(b, h) + aoff + m * 2048 + k * 1024); } while (0)
; #define PG8_LDB(dst, b, h) do { _Pragma("unroll") for (int n = 0; n < 2; ++n) _Pragma("unroll") for (int k = 0; k < 2; ++k) dst[n][k] = *(const LAS bf16x8*)(lds + PG8_SB(b, h) + boff + n * 2048 + k * 1024); } while (0)
; #define PG8_WAIT_L(n) asm volatile("s_waitcnt lgkmcnt(" #n ")" ::: "memory")
; #define PG8_BAR __builtin_amdgcn_s_barrier()
; #define PG8_SCHED __builtin_amdgcn_sched_barrier(0)
; #define PG8_WAIT_L(n) asm volatile("s_waitcnt lgkmcnt(" #n ")" ::: "memory")
; #define PG8_BAR __builtin_amdgcn_s_barrier()
; template <class Epi, class Sched, bool GATHER = false>
; __device__ __forceinline__ void gemm_phase(LAS unsigned char* lds, const Gemm g, const Sched& S, const Epi& E, const int* src = nullptr) {
;     ...
;         for (int t = 0; t < nt; t += 2) {
;             const bool last = (t == nt - 2);
;             const char* a1 = cA + (size_t)(t + 1) * kstep;
;             const char* a2 = last ? nA : cA + (size_t)(t + 2) * kstep; const char* b2 = last ? nB : cB + (size_t)(t + 2) * kstep;
;             const char* a3 = a2 + kstep; const char* b3 = b2 + kstep;
;             unsigned va2[2][2];
; #pragma unroll
;             for (int _h = 0; _h < 2; ++_h)
; #pragma unroll
;                 for (int _i = 0; _i < 2; ++_i) va2[_h][_i] = (GATHER && last) ? voffN[_h][_i] : voffA[_h][_i];
;             if (last && has_next) S.a_ready(nxt);
;             PG8_LDB(B0, 0, 0); PG8_SCHED; PG8_LDA(At, 0, 0); PG8_STAGE(PG8_SA(1, 1), a1 + cHA, voffA[1]);
;             PG8_WAIT_L(8); PG8_BAR; PG8_WAIT_L(0); PG8_MMA(0, 0, At, B0); PG8_BAR; PG8_SCHED;
;             PG8_LDB(B1, 0, 1); PG8_STAGE(PG8_SB(0, 0), b2, voffB);
;             PG8_BAR; PG8_WAIT_L(0); PG8_MMA(0, 1, At, B1); PG8_BAR;
;             if (full) PG8_LDA(At, 0, 1); PG8_STAGE(PG8_SA(0, 0), a2, va2[0]);
;             PG8_BAR; PG8_WAIT_L(0); if (full) PG8_MMA(1, 0, At, B0); PG8_BAR; PG8_SCHED;
.LBB0_1712:
	s_add_u32 s14, s94, s4
	s_addc_u32 s15, s95, s5
	s_add_u32 s16, s14, 0x3da00100
	ds_read_b128 v[162:165], v155
	ds_read_b128 v[166:169], v155 offset:1024
	ds_read_b128 v[170:173], v155 offset:2048
	ds_read_b128 v[174:177], v155 offset:3072
	s_addc_u32 s17, s15, 0
	s_add_u32 s45, s42, s4
	s_addc_u32 s46, s43, s5
	s_cmpk_eq_i32 s4, 0xf00
	s_cselect_b64 vcc, -1, 0
	s_and_b64 s[14:15], vcc, exec
	v_cndmask_b32_e32 v134, v141, v161, vcc
	s_cselect_b32 s17, s89, s17
	s_cselect_b32 s16, s88, s16
	v_cndmask_b32_e32 v226, v140, v160, vcc
	v_cndmask_b32_e32 v143, v142, v159, vcc
	v_cndmask_b32_e32 v145, v144, v158, vcc
	s_cselect_b32 s15, s11, s46
	s_cselect_b32 s14, s33, s45
	v_lshl_add_u64 v[210:211], v[148:149], 0, s[4:5]
	s_add_i32 m0, s23, 0xc000
	ds_read_b128 v[178:181], v156
	ds_read_b128 v[182:185], v156 offset:1024
	ds_read_b128 v[186:189], v156 offset:2048
	ds_read_b128 v[190:193], v156 offset:3072
	ds_read_b128 v[194:197], v156 offset:4096
	ds_read_b128 v[198:201], v156 offset:5120
	ds_read_b128 v[202:205], v156 offset:6144
	ds_read_b128 v[206:209], v156 offset:7168
	global_load_lds_dwordx4 v[210:211], off
	v_lshl_add_u64 v[210:211], v[146:147], 0, s[4:5]
	s_add_i32 m0, s23, 0xe000
	s_nop 0
	global_load_lds_dwordx4 v[210:211], off
	s_waitcnt lgkmcnt(8)
	s_barrier
	s_waitcnt lgkmcnt(0)
	s_setprio 1
	s_waitcnt lgkmcnt(0)
	v_mfma_f32_16x16x32_bf16 v[126:129], v[162:165], v[178:181], v[126:129]
	v_mfma_f32_16x16x32_bf16 v[122:125], v[170:173], v[178:181], v[122:125]
	v_mfma_f32_16x16x32_bf16 v[110:113], v[162:165], v[186:189], v[110:113]
	v_mfma_f32_16x16x32_bf16 v[106:109], v[170:173], v[186:189], v[106:109]
	v_mfma_f32_16x16x32_bf16 v[94:97], v[162:165], v[194:197], v[94:97]
	v_mfma_f32_16x16x32_bf16 v[90:93], v[170:173], v[194:197], v[90:93]
	v_mfma_f32_16x16x32_bf16 v[78:81], v[162:165], v[202:205], v[78:81]
	v_mfma_f32_16x16x32_bf16 v[74:77], v[170:173], v[202:205], v[74:77]
	v_mfma_f32_16x16x32_bf16 v[126:129], v[166:169], v[182:185], v[126:129]
	v_mfma_f32_16x16x32_bf16 v[122:125], v[174:177], v[182:185], v[122:125]
	v_mfma_f32_16x16x32_bf16 v[110:113], v[166:169], v[190:193], v[110:113]
	v_mfma_f32_16x16x32_bf16 v[106:109], v[174:177], v[190:193], v[106:109]
	v_mfma_f32_16x16x32_bf16 v[94:97], v[166:169], v[198:201], v[94:97]
	v_mfma_f32_16x16x32_bf16 v[90:93], v[174:177], v[198:201], v[90:93]
	v_mfma_f32_16x16x32_bf16 v[78:81], v[166:169], v[206:209], v[78:81]
	v_mfma_f32_16x16x32_bf16 v[74:77], v[174:177], v[206:209], v[74:77]
	s_setprio 0
	s_barrier
	s_add_i32 s45, s31, s21
	v_lshl_add_u64 v[230:231], s[14:15], 0, v[130:131]
	s_mov_b32 m0, s45
	ds_read_b128 v[210:213], v157
	ds_read_b128 v[214:217], v157 offset:1024
	ds_read_b128 v[218:221], v157 offset:2048
	ds_read_b128 v[222:225], v157 offset:3072
	global_load_lds_dwordx4 v[230:231], off
	v_lshl_add_u64 v[232:233], s[14:15], 0, v[132:133]
	s_add_i32 m0, s45, 0x2000
	s_nop 0
	global_load_lds_dwordx4 v[232:233], off
	s_barrier
	s_waitcnt lgkmcnt(0)
	s_setprio 1
	s_waitcnt lgkmcnt(0)
	v_mfma_f32_16x16x32_bf16 v[118:121], v[210:213], v[178:181], v[118:121]
	v_mfma_f32_16x16x32_bf16 v[114:117], v[218:221], v[178:181], v[114:117]
	v_mfma_f32_16x16x32_bf16 v[102:105], v[210:213], v[186:189], v[102:105]
	v_mfma_f32_16x16x32_bf16 v[98:101], v[218:221], v[186:189], v[98:101]
	v_mfma_f32_16x16x32_bf16 v[86:89], v[210:213], v[194:197], v[86:89]
	v_mfma_f32_16x16x32_bf16 v[82:85], v[218:221], v[194:197], v[82:85]
	v_mfma_f32_16x16x32_bf16 v[70:73], v[210:213], v[202:205], v[70:73]
	v_mfma_f32_16x16x32_bf16 v[66:69], v[218:221], v[202:205], v[66:69]
	v_mfma_f32_16x16x32_bf16 v[118:121], v[214:217], v[182:185], v[118:121]
	v_mfma_f32_16x16x32_bf16 v[114:117], v[222:225], v[182:185], v[114:117]
	v_mfma_f32_16x16x32_bf16 v[102:105], v[214:217], v[190:193], v[102:105]
	v_mfma_f32_16x16x32_bf16 v[98:101], v[222:225], v[190:193], v[98:101]
	v_mfma_f32_16x16x32_bf16 v[86:89], v[214:217], v[198:201], v[86:89]
	v_mfma_f32_16x16x32_bf16 v[82:85], v[222:225], v[198:201], v[82:85]
	v_mfma_f32_16x16x32_bf16 v[70:73], v[214:217], v[206:209], v[70:73]
	v_mfma_f32_16x16x32_bf16 v[66:69], v[222:225], v[206:209], v[66:69]
	s_setprio 0
	s_mov_b32 m0, s23
	s_barrier
	ds_read_b128 v[178:181], v156 offset:16384
	ds_read_b128 v[182:185], v156 offset:17408
	ds_read_b128 v[186:189], v156 offset:18432
	ds_read_b128 v[190:193], v156 offset:19456
	ds_read_b128 v[194:197], v156 offset:20480
	ds_read_b128 v[198:201], v156 offset:21504
	ds_read_b128 v[202:205], v156 offset:22528
	ds_read_b128 v[206:209], v156 offset:23552
	global_load_lds_dwordx4 v134, s[16:17]
	s_mov_b32 m0, s24
	v_mov_b32_e32 v227, v135
	global_load_lds_dwordx4 v226, s[16:17]
	s_barrier
	s_waitcnt lgkmcnt(0)
	v_lshl_add_u64 v[234:235], s[16:17], 0, v[134:135]
	v_lshl_add_u64 v[226:227], s[16:17], 0, v[226:227]
	s_setprio 1
	s_waitcnt lgkmcnt(0)
	v_mfma_f32_16x16x32_bf16 v[62:65], v[162:165], v[178:181], v[62:65]
	v_mfma_f32_16x16x32_bf16 v[58:61], v[170:173], v[178:181], v[58:61]
	v_mfma_f32_16x16x32_bf16 v[46:49], v[162:165], v[186:189], v[46:49]
	v_mfma_f32_16x16x32_bf16 v[42:45], v[170:173], v[186:189], v[42:45]
	v_mfma_f32_16x16x32_bf16 v[30:33], v[162:165], v[194:197], v[30:33]
	v_mfma_f32_16x16x32_bf16 v[26:29], v[170:173], v[194:197], v[26:29]
	v_mfma_f32_16x16x32_bf16 v[14:17], v[162:165], v[202:205], v[14:17]
	v_mfma_f32_16x16x32_bf16 v[10:13], v[170:173], v[202:205], v[10:13]
	v_mfma_f32_16x16x32_bf16 v[62:65], v[166:169], v[182:185], v[62:65]
	v_mfma_f32_16x16x32_bf16 v[58:61], v[174:177], v[182:185], v[58:61]
	v_mfma_f32_16x16x32_bf16 v[46:49], v[166:169], v[190:193], v[46:49]
	v_mfma_f32_16x16x32_bf16 v[42:45], v[174:177], v[190:193], v[42:45]
	v_mfma_f32_16x16x32_bf16 v[30:33], v[166:169], v[198:201], v[30:33]
	v_mfma_f32_16x16x32_bf16 v[26:29], v[174:177], v[198:201], v[26:29]
	v_mfma_f32_16x16x32_bf16 v[14:17], v[166:169], v[206:209], v[14:17]
	v_mfma_f32_16x16x32_bf16 v[10:13], v[174:177], v[206:209], v[10:13]
	s_setprio 0
	s_barrier
; #define PG8_STAGE(bufoff, gbase, voff) do { _Pragma("unroll") for (int _i = 0; _i < 2; ++_i) \
;         __builtin_amdgcn_global_load_lds((const unsigned*)((const char*)(gbase) + (voff)[_i]), (LAS unsigned*)(lds + (bufoff) + ldsw + _i * 8192), 16, 0, 0); } while (0)
; #define PG8_LDA(dst, b, h) do { _Pragma("unroll") for (int m = 0; m < 4; ++m) _Pragma("unroll") for (int k = 0; k < 2; ++k) dst[m][k] = *(const LAS bf16x8*)(lds + PG8_SA(b, h) + aoff + m * 2048 + k * 1024); } while (0)
; #define PG8_LDB(dst, b, h) do { _Pragma("unroll") for (int n = 0; n < 2; ++n) _Pragma("unroll") for (int k = 0; k < 2; ++k) dst[n][k] = *(const LAS bf16x8*)(lds + PG8_SB(b, h) + boff + n * 2048 + k * 1024); } while (0)
; #define PG8_MMA(ai, bj, At, Bt) do { __builtin_amdgcn_s_setprio(1); _Pragma("unroll") for (int m = 0; m < 4; ++m) _Pragma("unroll") for (int n = 0; n < 2; ++n) _Pragma("unroll") for (int k = 0; k < 2; ++k) \
;         acc[ai][bj][m][n] = __builtin_amdgcn_mfma_f32_16x16x32_bf16(Bt[n][k], At[m][k], acc[ai][bj][m][n], 0, 0, 0); __builtin_amdgcn_s_setprio(0); } while (0)
; #define PG8_WAIT_V(n) asm volatile("s_waitcnt vmcnt(" #n ")" ::: "memory")
; #define PG8_WAIT_L(n) asm volatile("s_waitcnt lgkmcnt(" #n ")" ::: "memory")
; #define PG8_BAR __builtin_amdgcn_s_barrier()
; #define PG8_SCHED __builtin_amdgcn_sched_barrier(0)
; #define PG8_WAIT_V(n) asm volatile("s_waitcnt vmcnt(" #n ")" ::: "memory")
; #define PG8_WAIT_L(n) asm volatile("s_waitcnt lgkmcnt(" #n ")" ::: "memory")
; template <class Epi, class Sched, bool GATHER = false>
; __device__ __forceinline__ void gemm_phase(LAS unsigned char* lds, const Gemm g, const Sched& S, const Epi& E, const int* src = nullptr) {
;     ...
;             PG8_STAGE(PG8_SB(0, 1), b2 + hstep, voffB);
;             PG8_WAIT_V(6); PG8_BAR; if (full) PG8_MMA(1, 1, At, B1); PG8_BAR;
;             PG8_LDB(B0, 1, 0); PG8_SCHED; PG8_LDA(At, 1, 0); PG8_STAGE(PG8_SA(0, 1), a2 + (last ? nHA : cHA), va2[1]);
;             PG8_WAIT_L(8); PG8_BAR; PG8_WAIT_L(0); PG8_MMA(0, 0, At, B0); PG8_BAR; PG8_SCHED;
;             PG8_LDB(B1, 1, 1); PG8_STAGE(PG8_SB(1, 0), b3, voffB);
;             PG8_BAR; PG8_WAIT_L(0); PG8_MMA(0, 1, At, B1); PG8_BAR;
;             if (full) PG8_LDA(At, 1, 1); PG8_STAGE(PG8_SA(1, 0), a3, va2[0]);
;             PG8_BAR; PG8_WAIT_L(0); if (full) PG8_MMA(1, 0, At, B0); PG8_BAR; PG8_SCHED;
	s_add_u32 s46, s14, 0x80000
	s_addc_u32 s47, s15, 0
	s_add_i32 s45, s34, s21
	v_lshl_add_u64 v[162:163], s[46:47], 0, v[130:131]
	s_mov_b32 m0, s45
	s_nop 0
	global_load_lds_dwordx4 v[162:163], off
	v_lshl_add_u64 v[162:163], s[46:47], 0, v[132:133]
	s_add_i32 m0, s45, 0x2000
	s_nop 0
	global_load_lds_dwordx4 v[162:163], off
	s_waitcnt vmcnt(6)
	v_lshl_or_b32 v240, v236, 12, v151
	v_lshl_or_b32 v241, v237, 12, v151
	v_lshl_or_b32 v242, v238, 12, v151
	v_lshl_or_b32 v243, v239, 12, v151
	v_cndmask_b32_e64 v161, v161, v240, s[64:65]
	v_cndmask_b32_e64 v160, v160, v241, s[64:65]
	v_cndmask_b32_e64 v159, v159, v242, s[64:65]
	v_cndmask_b32_e64 v158, v158, v243, s[64:65]
	s_barrier
	s_setprio 1
	v_mfma_f32_16x16x32_bf16 v[54:57], v[210:213], v[178:181], v[54:57]
	v_mfma_f32_16x16x32_bf16 v[50:53], v[218:221], v[178:181], v[50:53]
	v_mfma_f32_16x16x32_bf16 v[38:41], v[210:213], v[186:189], v[38:41]
	v_mfma_f32_16x16x32_bf16 v[34:37], v[218:221], v[186:189], v[34:37]
	v_mfma_f32_16x16x32_bf16 v[22:25], v[210:213], v[194:197], v[22:25]
	v_mfma_f32_16x16x32_bf16 v[18:21], v[218:221], v[194:197], v[18:21]
	v_mfma_f32_16x16x32_bf16 v[6:9], v[210:213], v[202:205], v[6:9]
	v_mfma_f32_16x16x32_bf16 v[2:5], v[218:221], v[202:205], v[2:5]
	v_mfma_f32_16x16x32_bf16 v[54:57], v[214:217], v[182:185], v[54:57]
	v_mfma_f32_16x16x32_bf16 v[50:53], v[222:225], v[182:185], v[50:53]
	v_mfma_f32_16x16x32_bf16 v[38:41], v[214:217], v[190:193], v[38:41]
	v_mfma_f32_16x16x32_bf16 v[34:37], v[222:225], v[190:193], v[34:37]
	v_mfma_f32_16x16x32_bf16 v[22:25], v[214:217], v[198:201], v[22:25]
	v_mfma_f32_16x16x32_bf16 v[18:21], v[222:225], v[198:201], v[18:21]
	v_mfma_f32_16x16x32_bf16 v[6:9], v[214:217], v[206:209], v[6:9]
	v_mfma_f32_16x16x32_bf16 v[2:5], v[222:225], v[206:209], v[2:5]
	s_setprio 0
	s_add_i32 s45, 0, 0x18000
	v_add_u32_e32 v134, s45, v153
	s_barrier
	ds_read_b128 v[162:165], v134
	ds_read_b128 v[166:169], v134 offset:1024
	ds_read_b128 v[170:173], v134 offset:2048
	ds_read_b128 v[174:177], v134 offset:3072
	s_mov_b32 m0, s25
	ds_read_b128 v[178:181], v156 offset:32768
	ds_read_b128 v[182:185], v156 offset:33792
	ds_read_b128 v[186:189], v156 offset:34816
	ds_read_b128 v[190:193], v156 offset:35840
	ds_read_b128 v[194:197], v156 offset:36864
	ds_read_b128 v[198:201], v156 offset:37888
	ds_read_b128 v[202:205], v156 offset:38912
	ds_read_b128 v[206:209], v156 offset:39936
	global_load_lds_dwordx4 v143, s[16:17]
	s_mov_b32 m0, s26
	s_nop 0
	global_load_lds_dwordx4 v145, s[16:17]
	s_waitcnt lgkmcnt(8)
	s_barrier
	s_waitcnt lgkmcnt(0)
	s_setprio 1
	s_waitcnt lgkmcnt(0)
	v_mfma_f32_16x16x32_bf16 v[126:129], v[162:165], v[178:181], v[126:129]
	v_mfma_f32_16x16x32_bf16 v[122:125], v[170:173], v[178:181], v[122:125]
	v_mfma_f32_16x16x32_bf16 v[110:113], v[162:165], v[186:189], v[110:113]
	v_mfma_f32_16x16x32_bf16 v[106:109], v[170:173], v[186:189], v[106:109]
	v_mfma_f32_16x16x32_bf16 v[94:97], v[162:165], v[194:197], v[94:97]
	v_mfma_f32_16x16x32_bf16 v[90:93], v[170:173], v[194:197], v[90:93]
	v_mfma_f32_16x16x32_bf16 v[78:81], v[162:165], v[202:205], v[78:81]
	v_mfma_f32_16x16x32_bf16 v[74:77], v[170:173], v[202:205], v[74:77]
	v_mfma_f32_16x16x32_bf16 v[126:129], v[166:169], v[182:185], v[126:129]
	v_mfma_f32_16x16x32_bf16 v[122:125], v[174:177], v[182:185], v[122:125]
	v_mfma_f32_16x16x32_bf16 v[110:113], v[166:169], v[190:193], v[110:113]
	v_mfma_f32_16x16x32_bf16 v[106:109], v[174:177], v[190:193], v[106:109]
	v_mfma_f32_16x16x32_bf16 v[94:97], v[166:169], v[198:201], v[94:97]
	v_mfma_f32_16x16x32_bf16 v[90:93], v[174:177], v[198:201], v[90:93]
	v_mfma_f32_16x16x32_bf16 v[78:81], v[166:169], v[206:209], v[78:81]
	v_mfma_f32_16x16x32_bf16 v[74:77], v[174:177], v[206:209], v[74:77]
	s_setprio 0
	s_barrier
	s_add_i32 s16, 0, 0x1c000
	s_add_i32 s17, s45, s21
	v_add_u32_e32 v134, s16, v153
	v_lshl_add_u64 v[230:231], v[230:231], 0, s[8:9]
	s_mov_b32 m0, s17
	ds_read_b128 v[210:213], v134
	ds_read_b128 v[214:217], v134 offset:1024
	ds_read_b128 v[218:221], v134 offset:2048
	ds_read_b128 v[222:225], v134 offset:3072
	global_load_lds_dwordx4 v[230:231], off
	v_lshl_add_u64 v[230:231], v[232:233], 0, s[8:9]
	s_add_i32 m0, s17, 0x2000
	s_nop 0
	global_load_lds_dwordx4 v[230:231], off
	s_barrier
	s_waitcnt lgkmcnt(0)
	s_setprio 1
	s_waitcnt lgkmcnt(0)
	v_mfma_f32_16x16x32_bf16 v[118:121], v[210:213], v[178:181], v[118:121]
	v_mfma_f32_16x16x32_bf16 v[114:117], v[218:221], v[178:181], v[114:117]
	v_mfma_f32_16x16x32_bf16 v[102:105], v[210:213], v[186:189], v[102:105]
	v_mfma_f32_16x16x32_bf16 v[98:101], v[218:221], v[186:189], v[98:101]
	v_mfma_f32_16x16x32_bf16 v[86:89], v[210:213], v[194:197], v[86:89]
	v_mfma_f32_16x16x32_bf16 v[82:85], v[218:221], v[194:197], v[82:85]
	v_mfma_f32_16x16x32_bf16 v[70:73], v[210:213], v[202:205], v[70:73]
	v_mfma_f32_16x16x32_bf16 v[66:69], v[218:221], v[202:205], v[66:69]
	v_mfma_f32_16x16x32_bf16 v[118:121], v[214:217], v[182:185], v[118:121]
	v_mfma_f32_16x16x32_bf16 v[114:117], v[222:225], v[182:185], v[114:117]
	v_mfma_f32_16x16x32_bf16 v[102:105], v[214:217], v[190:193], v[102:105]
	v_mfma_f32_16x16x32_bf16 v[98:101], v[222:225], v[190:193], v[98:101]
	v_mfma_f32_16x16x32_bf16 v[86:89], v[214:217], v[198:201], v[86:89]
	v_mfma_f32_16x16x32_bf16 v[82:85], v[222:225], v[198:201], v[82:85]
	v_mfma_f32_16x16x32_bf16 v[70:73], v[214:217], v[206:209], v[70:73]
	v_mfma_f32_16x16x32_bf16 v[66:69], v[222:225], v[206:209], v[66:69]
	s_setprio 0
	s_mov_b32 m0, s29
	v_lshl_add_u64 v[230:231], v[234:235], 0, s[8:9]
	s_barrier
; #define PG8_STAGE(bufoff, gbase, voff) do { _Pragma("unroll") for (int _i = 0; _i < 2; ++_i) \
;         __builtin_amdgcn_global_load_lds((const unsigned*)((const char*)(gbase) + (voff)[_i]), (LAS unsigned*)(lds + (bufoff) + ldsw + _i * 8192), 16, 0, 0); } while (0)
; #define PG8_LDA(dst, b, h) do { _Pragma("unroll") for (int m = 0; m < 4; ++m) _Pragma("unroll") for (int k = 0; k < 2; ++k) dst[m][k] = *(const LAS bf16x8*)(lds + PG8_SA(b, h) + aoff + m * 2048 + k * 1024); } while (0)
; #define PG8_LDB(dst, b, h) do { _Pragma("unroll") for (int n = 0; n < 2; ++n) _Pragma("unroll") for (int k = 0; k < 2; ++k) dst[n][k] = *(const LAS bf16x8*)(lds + PG8_SB(b, h) + boff + n * 2048 + k * 1024); } while (0)
; template <class Epi, class Sched, bool GATHER = false>
; __device__ __forceinline__ void gemm_phase(LAS unsigned char* lds, const Gemm g, const Sched& S, const Epi& E, const int* src = nullptr) {
;     ...
;             PG8_WAIT_L(8); PG8_BAR; PG8_WAIT_L(0); PG8_MMA(0, 0, At, B0); PG8_BAR; PG8_SCHED;
;             PG8_LDB(B1, 1, 1); PG8_STAGE(PG8_SB(1, 0), b3, voffB);
;             PG8_BAR; PG8_WAIT_L(0); PG8_MMA(0, 1, At, B1); PG8_BAR;
;             if (full) PG8_LDA(At, 1, 1); PG8_STAGE(PG8_SA(1, 0), a3, va2[0]);
;             PG8_BAR; PG8_WAIT_L(0); if (full) PG8_MMA(1, 0, At, B0); PG8_BAR; PG8_SCHED;
;             PG8_STAGE(PG8_SB(1, 1), b3 + hstep, voffB);
;             PG8_WAIT_V(6); PG8_BAR; if (full) PG8_MMA(1, 1, At, B1); PG8_BAR;
;     __device__ __forceinline__ void operator()(const f32x4 (&acc)[2][2][4][2], const Unit& u, int wr, int wc, int fr, int fq) const {
;         const int row0 = u.pm * BM + (u.hf == 2 ? HALF : 0) + wr * 64 + fr, col0 = u.pc * HALF + wc * 32 + 8 * fq;
; #pragma unroll
;         for (int ai = 0; ai < 2; ++ai) if (ai == 0 || u.hf == 0)
; #pragma unroll
;             for (int m = 0; m < 4; ++m) { bf16_t* rowp = O + (size_t)(row0 + ai * HALF + m * 16) * D + col0;
;                 float h[8];
; #pragma unroll
;                 for (int n = 0; n < 2; ++n)
; #pragma unroll
;                     for (int j = 0; j < 4; ++j) { const float gt = acc[ai][0][m][n][j], up = acc[ai][1][m][n][j]; h[n * 4 + j] = gt * __builtin_amdgcn_rcpf(1.f + __expf(-gt)) * up; }
;                 u32x4 w; w.x = pk2(h[0], h[1]); w.y = pk2(h[2], h[3]); w.z = pk2(h[4], h[5]); w.w = pk2(h[6], h[7]);
;                 *(u32x4*)rowp = w; }
	ds_read_b128 v[178:181], v156 offset:49152
	ds_read_b128 v[182:185], v156 offset:50176
	ds_read_b128 v[186:189], v156 offset:51200
	ds_read_b128 v[190:193], v156 offset:52224
	ds_read_b128 v[194:197], v156 offset:53248
	ds_read_b128 v[198:201], v156 offset:54272
	ds_read_b128 v[202:205], v156 offset:55296
	ds_read_b128 v[206:209], v156 offset:56320
	global_load_lds_dwordx4 v[230:231], off
	v_lshl_add_u64 v[226:227], v[226:227], 0, s[8:9]
	s_mov_b32 m0, s30
	s_nop 0
	global_load_lds_dwordx4 v[226:227], off
	s_barrier
	s_waitcnt lgkmcnt(0)
	s_setprio 1
	s_waitcnt lgkmcnt(0)
	v_mfma_f32_16x16x32_bf16 v[62:65], v[162:165], v[178:181], v[62:65]
	v_mfma_f32_16x16x32_bf16 v[58:61], v[170:173], v[178:181], v[58:61]
	v_mfma_f32_16x16x32_bf16 v[46:49], v[162:165], v[186:189], v[46:49]
	v_mfma_f32_16x16x32_bf16 v[42:45], v[170:173], v[186:189], v[42:45]
	v_mfma_f32_16x16x32_bf16 v[30:33], v[162:165], v[194:197], v[30:33]
	v_mfma_f32_16x16x32_bf16 v[26:29], v[170:173], v[194:197], v[26:29]
	v_mfma_f32_16x16x32_bf16 v[14:17], v[162:165], v[202:205], v[14:17]
	v_mfma_f32_16x16x32_bf16 v[10:13], v[170:173], v[202:205], v[10:13]
	v_mfma_f32_16x16x32_bf16 v[62:65], v[166:169], v[182:185], v[62:65]
	v_mfma_f32_16x16x32_bf16 v[58:61], v[174:177], v[182:185], v[58:61]
	v_mfma_f32_16x16x32_bf16 v[46:49], v[166:169], v[190:193], v[46:49]
	v_mfma_f32_16x16x32_bf16 v[42:45], v[174:177], v[190:193], v[42:45]
	v_mfma_f32_16x16x32_bf16 v[30:33], v[166:169], v[198:201], v[30:33]
	v_mfma_f32_16x16x32_bf16 v[26:29], v[174:177], v[198:201], v[26:29]
	v_mfma_f32_16x16x32_bf16 v[14:17], v[166:169], v[206:209], v[14:17]
	v_mfma_f32_16x16x32_bf16 v[10:13], v[174:177], v[206:209], v[10:13]
	s_setprio 0
	s_barrier
	s_add_u32 s14, s14, 0x80080
	s_addc_u32 s15, s15, 0
	s_add_i32 s16, s16, s21
	v_lshl_add_u64 v[162:163], s[14:15], 0, v[130:131]
	s_mov_b32 m0, s16
	s_nop 0
	global_load_lds_dwordx4 v[162:163], off
	v_lshl_add_u64 v[162:163], s[14:15], 0, v[132:133]
	s_add_i32 m0, s16, 0x2000
	s_nop 0
	global_load_lds_dwordx4 v[162:163], off
	s_waitcnt vmcnt(6)
	s_barrier
	s_setprio 1
	v_mfma_f32_16x16x32_bf16 v[54:57], v[210:213], v[178:181], v[54:57]
	v_mfma_f32_16x16x32_bf16 v[50:53], v[218:221], v[178:181], v[50:53]
	v_mfma_f32_16x16x32_bf16 v[38:41], v[210:213], v[186:189], v[38:41]
	v_mfma_f32_16x16x32_bf16 v[34:37], v[218:221], v[186:189], v[34:37]
	v_mfma_f32_16x16x32_bf16 v[22:25], v[210:213], v[194:197], v[22:25]
	v_mfma_f32_16x16x32_bf16 v[18:21], v[218:221], v[194:197], v[18:21]
	v_mfma_f32_16x16x32_bf16 v[6:9], v[210:213], v[202:205], v[6:9]
	v_mfma_f32_16x16x32_bf16 v[2:5], v[218:221], v[202:205], v[2:5]
	v_mfma_f32_16x16x32_bf16 v[54:57], v[214:217], v[182:185], v[54:57]
	v_mfma_f32_16x16x32_bf16 v[50:53], v[222:225], v[182:185], v[50:53]
	v_mfma_f32_16x16x32_bf16 v[38:41], v[214:217], v[190:193], v[38:41]
	v_mfma_f32_16x16x32_bf16 v[34:37], v[222:225], v[190:193], v[34:37]
	v_mfma_f32_16x16x32_bf16 v[22:25], v[214:217], v[198:201], v[22:25]
	v_mfma_f32_16x16x32_bf16 v[18:21], v[222:225], v[198:201], v[18:21]
	v_mfma_f32_16x16x32_bf16 v[6:9], v[214:217], v[206:209], v[6:9]
	v_mfma_f32_16x16x32_bf16 v[2:5], v[222:225], v[206:209], v[2:5]
	s_setprio 0
	s_add_i32 s44, s44, 2
	s_add_u32 s4, s4, 0x100
	s_addc_u32 s5, s5, 0
	s_cmp_gt_u32 s44, 29
	s_barrier
	s_cbranch_scc0 .LBB0_1712
	v_lshl_add_u32 v142, s41, 8, v152
	v_ashrrev_i32_e32 v143, 31, v142
	v_mul_f32_e32 v134, 0xbfb8aa3b, v126
	v_lshlrev_b64 v[144:145], 12, v[142:143]
	v_exp_f32_e32 v134, v134
	v_mul_f32_e32 v143, 0xbfb8aa3b, v127
	v_exp_f32_e32 v143, v143
	v_mul_f32_e32 v147, 0xbfb8aa3b, v129
	v_add_f32_e32 v134, 1.0, v134
	v_rcp_f32_e32 v146, v134
	v_add_f32_e32 v134, 1.0, v143
	v_mul_f32_e32 v143, 0xbfb8aa3b, v128
	v_exp_f32_e32 v143, v143
	v_exp_f32_e32 v149, v147
	v_rcp_f32_e32 v147, v134
	v_lshl_or_b32 v140, s40, 7, v154
	v_add_f32_e32 v134, 1.0, v143
	v_mul_f32_e32 v143, 0xbfb8aa3b, v122
	v_rcp_f32_e32 v148, v134
	v_add_f32_e32 v134, 1.0, v149
	v_exp_f32_e32 v143, v143
	v_mul_f32_e32 v149, 0xbfb8aa3b, v123
	v_exp_f32_e32 v163, v149
	v_rcp_f32_e32 v149, v134
	v_add_f32_e32 v134, 1.0, v143
	v_mul_f32_e32 v143, 0xbfb8aa3b, v124
	v_rcp_f32_e32 v162, v134
	v_add_f32_e32 v134, 1.0, v163
	v_exp_f32_e32 v143, v143
	v_mul_f32_e32 v163, 0xbfb8aa3b, v125
	v_exp_f32_e32 v165, v163
	v_rcp_f32_e32 v163, v134
	v_add_f32_e32 v134, 1.0, v143
	v_rcp_f32_e32 v164, v134
	v_add_f32_e32 v134, 1.0, v165
	v_pk_mul_f32 v[126:127], v[126:127], v[146:147]
	v_rcp_f32_e32 v165, v134
	v_pk_mul_f32 v[118:119], v[126:127], v[118:119]
	v_pk_mul_f32 v[126:127], v[128:129], v[148:149]
	v_cvt_pk_bf16_f32 v118, v118, v119
	v_pk_mul_f32 v[120:121], v[126:127], v[120:121]
	v_ashrrev_i32_e32 v141, 31, v140
	v_cvt_pk_bf16_f32 v119, v120, v121
	v_pk_mul_f32 v[120:121], v[122:123], v[162:163]
	v_lshl_add_u64 v[144:145], s[76:77], 0, v[144:145]
	v_pk_mul_f32 v[114:115], v[120:121], v[114:115]
	v_lshlrev_b64 v[166:167], 1, v[140:141]
	v_cvt_pk_bf16_f32 v120, v114, v115
	v_pk_mul_f32 v[114:115], v[124:125], v[164:165]
	v_lshl_add_u64 v[140:141], v[144:145], 0, v[166:167]
	v_pk_mul_f32 v[114:115], v[114:115], v[116:117]
	v_mul_f32_e32 v116, 0xbfb8aa3b, v110
	v_cvt_pk_bf16_f32 v121, v114, v115
	v_mul_f32_e32 v117, 0xbfb8aa3b, v111
	global_store_dwordx4 v[140:141], v[118:121], off
	v_exp_f32_e32 v116, v116
	v_exp_f32_e32 v117, v117
	v_mul_f32_e32 v118, 0xbfb8aa3b, v112
	v_mul_f32_e32 v119, 0xbfb8aa3b, v113
	v_exp_f32_e32 v118, v118
	v_exp_f32_e32 v119, v119
	v_mul_f32_e32 v120, 0xbfb8aa3b, v106
	v_mul_f32_e32 v121, 0xbfb8aa3b, v107
	v_exp_f32_e32 v120, v120
	v_exp_f32_e32 v121, v121
	v_add_f32_e32 v116, 1.0, v116
	v_add_f32_e32 v117, 1.0, v117
;     __device__ __forceinline__ void operator()(const f32x4 (&acc)[2][2][4][2], const Unit& u, int wr, int wc, int fr, int fq) const {
;         const int row0 = u.pm * BM + (u.hf == 2 ? HALF : 0) + wr * 64 + fr, col0 = u.pc * HALF + wc * 32 + 8 * fq;
; #pragma unroll
;         for (int ai = 0; ai < 2; ++ai) if (ai == 0 || u.hf == 0)
; #pragma unroll
;             for (int m = 0; m < 4; ++m) { bf16_t* rowp = O + (size_t)(row0 + ai * HALF + m * 16) * D + col0;
;                 float h[8];
; #pragma unroll
;                 for (int n = 0; n < 2; ++n)
; #pragma unroll
;                     for (int j = 0; j < 4; ++j) { const float gt = acc[ai][0][m][n][j], up = acc[ai][1][m][n][j]; h[n * 4 + j] = gt * __builtin_amdgcn_rcpf(1.f + __expf(-gt)) * up; }
;                 u32x4 w; w.x = pk2(h[0], h[1]); w.y = pk2(h[2], h[3]); w.z = pk2(h[4], h[5]); w.w = pk2(h[6], h[7]);
;                 *(u32x4*)rowp = w; }
	v_mul_f32_e32 v122, 0xbfb8aa3b, v108
	v_mul_f32_e32 v123, 0xbfb8aa3b, v109
	v_rcp_f32_e32 v116, v116
	v_rcp_f32_e32 v117, v117
	v_add_f32_e32 v118, 1.0, v118
	v_add_f32_e32 v119, 1.0, v119
	v_exp_f32_e32 v122, v122
	v_exp_f32_e32 v123, v123
	v_rcp_f32_e32 v118, v118
	v_rcp_f32_e32 v119, v119
	v_add_f32_e32 v120, 1.0, v120
	v_add_f32_e32 v121, 1.0, v121
	v_rcp_f32_e32 v120, v120
	v_rcp_f32_e32 v121, v121
	v_add_f32_e32 v122, 1.0, v122
	v_add_f32_e32 v123, 1.0, v123
	v_pk_mul_f32 v[110:111], v[110:111], v[116:117]
	v_rcp_f32_e32 v122, v122
	v_rcp_f32_e32 v123, v123
	v_pk_mul_f32 v[102:103], v[110:111], v[102:103]
	v_pk_mul_f32 v[110:111], v[112:113], v[118:119]
	v_or_b32_e32 v114, 16, v142
	v_pk_mul_f32 v[104:105], v[110:111], v[104:105]
	v_cvt_pk_bf16_f32 v102, v102, v103
	v_cvt_pk_bf16_f32 v103, v104, v105
	v_pk_mul_f32 v[104:105], v[106:107], v[120:121]
	v_ashrrev_i32_e32 v115, 31, v114
	v_pk_mul_f32 v[98:99], v[104:105], v[98:99]
	v_lshlrev_b64 v[114:115], 12, v[114:115]
	v_cvt_pk_bf16_f32 v104, v98, v99
	v_pk_mul_f32 v[98:99], v[108:109], v[122:123]
	v_lshl_add_u64 v[114:115], s[76:77], 0, v[114:115]
	v_pk_mul_f32 v[98:99], v[98:99], v[100:101]
	v_lshl_add_u64 v[114:115], v[114:115], 0, v[166:167]
	v_cvt_pk_bf16_f32 v105, v98, v99
	v_mul_f32_e32 v100, 0xbfb8aa3b, v94
	v_mul_f32_e32 v101, 0xbfb8aa3b, v95
	global_store_dwordx4 v[114:115], v[102:105], off
	v_exp_f32_e32 v100, v100
	v_exp_f32_e32 v101, v101
	v_mul_f32_e32 v102, 0xbfb8aa3b, v96
	v_mul_f32_e32 v103, 0xbfb8aa3b, v97
	v_exp_f32_e32 v102, v102
	v_exp_f32_e32 v103, v103
	v_mul_f32_e32 v104, 0xbfb8aa3b, v90
	v_mul_f32_e32 v105, 0xbfb8aa3b, v91
	v_exp_f32_e32 v104, v104
	v_exp_f32_e32 v105, v105
	v_add_f32_e32 v100, 1.0, v100
	v_add_f32_e32 v101, 1.0, v101
	v_mul_f32_e32 v106, 0xbfb8aa3b, v92
	v_mul_f32_e32 v107, 0xbfb8aa3b, v93
	v_rcp_f32_e32 v100, v100
	v_rcp_f32_e32 v101, v101
	v_add_f32_e32 v102, 1.0, v102
	v_add_f32_e32 v103, 1.0, v103
	v_exp_f32_e32 v106, v106
	v_exp_f32_e32 v107, v107
	v_rcp_f32_e32 v102, v102
	v_rcp_f32_e32 v103, v103
	v_add_f32_e32 v104, 1.0, v104
	v_add_f32_e32 v105, 1.0, v105
	v_rcp_f32_e32 v104, v104
	v_rcp_f32_e32 v105, v105
	v_add_f32_e32 v106, 1.0, v106
	v_add_f32_e32 v107, 1.0, v107
	v_pk_mul_f32 v[94:95], v[94:95], v[100:101]
	v_rcp_f32_e32 v106, v106
	v_rcp_f32_e32 v107, v107
	v_pk_mul_f32 v[86:87], v[94:95], v[86:87]
	v_pk_mul_f32 v[94:95], v[96:97], v[102:103]
	v_or_b32_e32 v98, 32, v142
	v_pk_mul_f32 v[88:89], v[94:95], v[88:89]
	v_cvt_pk_bf16_f32 v86, v86, v87
	v_cvt_pk_bf16_f32 v87, v88, v89
	v_pk_mul_f32 v[88:89], v[90:91], v[104:105]
	v_ashrrev_i32_e32 v99, 31, v98
	v_pk_mul_f32 v[82:83], v[88:89], v[82:83]
	v_lshlrev_b64 v[98:99], 12, v[98:99]
	v_cvt_pk_bf16_f32 v88, v82, v83
	v_pk_mul_f32 v[82:83], v[92:93], v[106:107]
	v_lshl_add_u64 v[98:99], s[76:77], 0, v[98:99]
	v_pk_mul_f32 v[82:83], v[82:83], v[84:85]
	v_lshl_add_u64 v[98:99], v[98:99], 0, v[166:167]
	v_cvt_pk_bf16_f32 v89, v82, v83
	v_mul_f32_e32 v84, 0xbfb8aa3b, v78
	v_mul_f32_e32 v85, 0xbfb8aa3b, v79
	global_store_dwordx4 v[98:99], v[86:89], off
	v_exp_f32_e32 v84, v84
	v_exp_f32_e32 v85, v85
	v_mul_f32_e32 v86, 0xbfb8aa3b, v80
	v_mul_f32_e32 v87, 0xbfb8aa3b, v81
	v_exp_f32_e32 v86, v86
	v_exp_f32_e32 v87, v87
	v_mul_f32_e32 v88, 0xbfb8aa3b, v74
	v_mul_f32_e32 v89, 0xbfb8aa3b, v75
	v_exp_f32_e32 v88, v88
	v_exp_f32_e32 v89, v89
	v_add_f32_e32 v84, 1.0, v84
	v_add_f32_e32 v85, 1.0, v85
	v_mul_f32_e32 v90, 0xbfb8aa3b, v76
	v_mul_f32_e32 v91, 0xbfb8aa3b, v77
	v_rcp_f32_e32 v84, v84
	v_rcp_f32_e32 v85, v85
	v_add_f32_e32 v86, 1.0, v86
	v_add_f32_e32 v87, 1.0, v87
	v_exp_f32_e32 v90, v90
	v_exp_f32_e32 v91, v91
	v_rcp_f32_e32 v86, v86
	v_rcp_f32_e32 v87, v87
	v_add_f32_e32 v88, 1.0, v88
	v_add_f32_e32 v89, 1.0, v89
	v_rcp_f32_e32 v88, v88
	v_rcp_f32_e32 v89, v89
	v_add_f32_e32 v90, 1.0, v90
	v_add_f32_e32 v91, 1.0, v91
	v_pk_mul_f32 v[78:79], v[78:79], v[84:85]
	v_rcp_f32_e32 v90, v90
	v_rcp_f32_e32 v91, v91
	v_pk_mul_f32 v[70:71], v[78:79], v[70:71]
	v_pk_mul_f32 v[78:79], v[80:81], v[86:87]
	v_cvt_pk_bf16_f32 v70, v70, v71
	v_pk_mul_f32 v[72:73], v[78:79], v[72:73]
	v_or_b32_e32 v82, 48, v142
	v_cvt_pk_bf16_f32 v71, v72, v73
	v_pk_mul_f32 v[72:73], v[74:75], v[88:89]
	v_ashrrev_i32_e32 v83, 31, v82
	v_pk_mul_f32 v[66:67], v[72:73], v[66:67]
	v_lshlrev_b64 v[82:83], 12, v[82:83]
	v_cvt_pk_bf16_f32 v72, v66, v67
	v_pk_mul_f32 v[66:67], v[76:77], v[90:91]
	v_lshl_add_u64 v[82:83], s[76:77], 0, v[82:83]
	v_pk_mul_f32 v[66:67], v[66:67], v[68:69]
	v_mul_f32_e32 v68, 0xbfb8aa3b, v64
	v_cvt_pk_bf16_f32 v73, v66, v67
	v_mul_f32_e32 v66, 0xbfb8aa3b, v62
	v_mul_f32_e32 v67, 0xbfb8aa3b, v63
	v_exp_f32_e32 v66, v66
	v_exp_f32_e32 v67, v67
	v_mul_f32_e32 v69, 0xbfb8aa3b, v65
	v_lshl_add_u64 v[82:83], v[82:83], 0, v[166:167]
	v_exp_f32_e32 v68, v68
	v_exp_f32_e32 v69, v69
	global_store_dwordx4 v[82:83], v[70:73], off
	v_add_f32_e32 v66, 1.0, v66
	v_add_f32_e32 v67, 1.0, v67
	v_mul_f32_e32 v70, 0xbfb8aa3b, v58
	v_mul_f32_e32 v71, 0xbfb8aa3b, v59
	v_exp_f32_e32 v70, v70
	v_exp_f32_e32 v71, v71
	v_mul_f32_e32 v72, 0xbfb8aa3b, v60
	v_mul_f32_e32 v73, 0xbfb8aa3b, v61
	v_rcp_f32_e32 v66, v66
	v_rcp_f32_e32 v67, v67
	v_add_f32_e32 v68, 1.0, v68
	v_add_f32_e32 v69, 1.0, v69
	v_exp_f32_e32 v72, v72
	v_exp_f32_e32 v73, v73
	v_rcp_f32_e32 v68, v68
	v_rcp_f32_e32 v69, v69
	v_add_f32_e32 v70, 1.0, v70
	v_add_f32_e32 v71, 1.0, v71
	v_rcp_f32_e32 v70, v70
	v_rcp_f32_e32 v71, v71
	v_add_f32_e32 v72, 1.0, v72
	v_add_f32_e32 v73, 1.0, v73
	v_pk_mul_f32 v[62:63], v[62:63], v[66:67]
	v_rcp_f32_e32 v72, v72
; #define PG8_WAIT_V(n) asm volatile("s_waitcnt vmcnt(" #n ")" ::: "memory")
; #define PG8_BAR __builtin_amdgcn_s_barrier()
; #define PG8_WAIT_V(n) asm volatile("s_waitcnt vmcnt(" #n ")" ::: "memory")
; #define PG8_BAR __builtin_amdgcn_s_barrier()
; template <class Epi, class Sched, bool GATHER = false>
; __device__ __forceinline__ void gemm_phase(LAS unsigned char* lds, const Gemm g, const Sched& S, const Epi& E, const int* src = nullptr) {
;     ...
;         E(acc, cur, wr, wc, fr, fq); S.done(cur);
;         if (!has_next) break;
; #pragma unroll
;         for (int a = 0; a < 2; ++a)
; #pragma unroll
;             for (int b = 0; b < 2; ++b)
; #pragma unroll
;                 for (int m = 0; m < 4; ++m)
; #pragma unroll
;                     for (int n = 0; n < 2; ++n) acc[a][b][m][n] = (f32x4){0.f, 0.f, 0.f, 0.f};
;         cur = nxt; cA = nA; cB = nB; cHA = nHA; full = cur.hf == 0; ++ui;
;         if (GATHER) {
; #pragma unroll
;             for (int _h = 0; _h < 2; ++_h)
; #pragma unroll
;                 for (int _i = 0; _i < 2; ++_i) voffA[_h][_i] = voffN[_h][_i]; }
;     }
;     PG8_WAIT_V(0);
;     if (wr == 0) PG8_BAR;
;     PG8_BAR;
;     __device__ __forceinline__ void operator()(const f32x4 (&acc)[2][2][4][2], const Unit& u, int wr, int wc, int fr, int fq) const {
;         const int row0 = u.pm * BM + (u.hf == 2 ? HALF : 0) + wr * 64 + fr, col0 = u.pc * HALF + wc * 32 + 8 * fq;
; #pragma unroll
;         for (int ai = 0; ai < 2; ++ai) if (ai == 0 || u.hf == 0)
; #pragma unroll
;             for (int m = 0; m < 4; ++m) { bf16_t* rowp = O + (size_t)(row0 + ai * HALF + m * 16) * D + col0;
;                 float h[8];
; #pragma unroll
;                 for (int n = 0; n < 2; ++n)
; #pragma unroll
;                     for (int j = 0; j < 4; ++j) { const float gt = acc[ai][0][m][n][j], up = acc[ai][1][m][n][j]; h[n * 4 + j] = gt * __builtin_amdgcn_rcpf(1.f + __expf(-gt)) * up; }
;                 u32x4 w; w.x = pk2(h[0], h[1]); w.y = pk2(h[2], h[3]); w.z = pk2(h[4], h[5]); w.w = pk2(h[6], h[7]);
;                 *(u32x4*)rowp = w; }
	v_rcp_f32_e32 v73, v73
	v_pk_mul_f32 v[54:55], v[62:63], v[54:55]
	v_pk_mul_f32 v[62:63], v[64:65], v[68:69]
	v_cvt_pk_bf16_f32 v54, v54, v55
	v_pk_mul_f32 v[56:57], v[62:63], v[56:57]
	v_mov_b32_e32 v142, v159
	v_cvt_pk_bf16_f32 v55, v56, v57
	v_pk_mul_f32 v[56:57], v[58:59], v[70:71]
	v_mov_b32_e32 v144, v158
	v_pk_mul_f32 v[50:51], v[56:57], v[50:51]
	s_mov_b32 s40, s38
	v_cvt_pk_bf16_f32 v56, v50, v51
	v_pk_mul_f32 v[50:51], v[60:61], v[72:73]
	s_mov_b32 s41, s39
	v_pk_mul_f32 v[50:51], v[50:51], v[52:53]
	v_mul_f32_e32 v52, 0xbfb8aa3b, v46
	v_mul_f32_e32 v53, 0xbfb8aa3b, v47
	v_exp_f32_e32 v52, v52
	v_exp_f32_e32 v53, v53
	v_cvt_pk_bf16_f32 v57, v50, v51
	v_add_co_u32_e32 v50, vcc, s35, v140
	s_mov_b64 s[14:15], s[12:13]
	s_nop 0
	v_addc_co_u32_e32 v51, vcc, 0, v141, vcc
	global_store_dwordx4 v[50:51], v[54:57], off
	v_add_f32_e32 v50, 1.0, v52
	v_add_f32_e32 v51, 1.0, v53
	v_mul_f32_e32 v52, 0xbfb8aa3b, v48
	v_mul_f32_e32 v53, 0xbfb8aa3b, v49
	v_exp_f32_e32 v52, v52
	v_exp_f32_e32 v53, v53
	v_mul_f32_e32 v54, 0xbfb8aa3b, v42
	v_mul_f32_e32 v55, 0xbfb8aa3b, v43
	v_exp_f32_e32 v54, v54
	v_exp_f32_e32 v55, v55
	v_mul_f32_e32 v56, 0xbfb8aa3b, v44
	v_mul_f32_e32 v57, 0xbfb8aa3b, v45
	v_rcp_f32_e32 v50, v50
	v_rcp_f32_e32 v51, v51
	v_add_f32_e32 v52, 1.0, v52
	v_add_f32_e32 v53, 1.0, v53
	v_exp_f32_e32 v56, v56
	v_exp_f32_e32 v57, v57
	v_rcp_f32_e32 v52, v52
	v_rcp_f32_e32 v53, v53
	v_add_f32_e32 v54, 1.0, v54
	v_add_f32_e32 v55, 1.0, v55
	v_rcp_f32_e32 v54, v54
	v_rcp_f32_e32 v55, v55
	v_add_f32_e32 v56, 1.0, v56
	v_add_f32_e32 v57, 1.0, v57
	v_pk_mul_f32 v[46:47], v[46:47], v[50:51]
	v_rcp_f32_e32 v56, v56
	v_rcp_f32_e32 v57, v57
	v_pk_mul_f32 v[38:39], v[46:47], v[38:39]
	v_pk_mul_f32 v[46:47], v[48:49], v[52:53]
	v_cvt_pk_bf16_f32 v38, v38, v39
	v_pk_mul_f32 v[40:41], v[46:47], v[40:41]
	s_nop 0
	v_cvt_pk_bf16_f32 v39, v40, v41
	v_pk_mul_f32 v[40:41], v[42:43], v[54:55]
	s_nop 0
	v_pk_mul_f32 v[34:35], v[40:41], v[34:35]
	s_nop 0
	v_cvt_pk_bf16_f32 v40, v34, v35
	v_pk_mul_f32 v[34:35], v[44:45], v[56:57]
	s_nop 0
	v_pk_mul_f32 v[34:35], v[34:35], v[36:37]
	v_mul_f32_e32 v36, 0xbfb8aa3b, v30
	v_mul_f32_e32 v37, 0xbfb8aa3b, v31
	v_exp_f32_e32 v36, v36
	v_exp_f32_e32 v37, v37
	v_cvt_pk_bf16_f32 v41, v34, v35
	v_add_co_u32_e32 v34, vcc, s36, v140
	s_nop 1
	v_addc_co_u32_e32 v35, vcc, 0, v141, vcc
	global_store_dwordx4 v[34:35], v[38:41], off
	v_add_f32_e32 v34, 1.0, v36
	v_add_f32_e32 v35, 1.0, v37
	v_mul_f32_e32 v36, 0xbfb8aa3b, v32
	v_mul_f32_e32 v37, 0xbfb8aa3b, v33
	v_exp_f32_e32 v36, v36
	v_exp_f32_e32 v37, v37
	v_mul_f32_e32 v38, 0xbfb8aa3b, v26
	v_mul_f32_e32 v39, 0xbfb8aa3b, v27
	v_exp_f32_e32 v38, v38
	v_exp_f32_e32 v39, v39
	v_mul_f32_e32 v40, 0xbfb8aa3b, v28
	v_mul_f32_e32 v41, 0xbfb8aa3b, v29
	v_rcp_f32_e32 v34, v34
	v_rcp_f32_e32 v35, v35
	v_add_f32_e32 v36, 1.0, v36
	v_add_f32_e32 v37, 1.0, v37
	v_exp_f32_e32 v40, v40
	v_exp_f32_e32 v41, v41
	v_rcp_f32_e32 v36, v36
	v_rcp_f32_e32 v37, v37
	v_add_f32_e32 v38, 1.0, v38
	v_add_f32_e32 v39, 1.0, v39
	v_rcp_f32_e32 v38, v38
	v_rcp_f32_e32 v39, v39
	v_add_f32_e32 v40, 1.0, v40
	v_add_f32_e32 v41, 1.0, v41
	v_pk_mul_f32 v[30:31], v[30:31], v[34:35]
	v_rcp_f32_e32 v40, v40
	v_rcp_f32_e32 v41, v41
	v_pk_mul_f32 v[22:23], v[30:31], v[22:23]
	v_pk_mul_f32 v[30:31], v[32:33], v[36:37]
	v_cvt_pk_bf16_f32 v22, v22, v23
	v_pk_mul_f32 v[24:25], v[30:31], v[24:25]
	s_nop 0
	v_cvt_pk_bf16_f32 v23, v24, v25
	v_pk_mul_f32 v[24:25], v[26:27], v[38:39]
	s_nop 0
	v_pk_mul_f32 v[18:19], v[24:25], v[18:19]
	s_nop 0
	v_cvt_pk_bf16_f32 v24, v18, v19
	v_pk_mul_f32 v[18:19], v[28:29], v[40:41]
	s_nop 0
	v_pk_mul_f32 v[18:19], v[18:19], v[20:21]
	v_mul_f32_e32 v20, 0xbfb8aa3b, v14
	v_mul_f32_e32 v21, 0xbfb8aa3b, v15
	v_exp_f32_e32 v20, v20
	v_exp_f32_e32 v21, v21
	v_cvt_pk_bf16_f32 v25, v18, v19
	v_add_co_u32_e32 v18, vcc, s37, v140
	s_nop 1
	v_addc_co_u32_e32 v19, vcc, 0, v141, vcc
	global_store_dwordx4 v[18:19], v[22:25], off
	v_add_f32_e32 v18, 1.0, v20
	v_add_f32_e32 v19, 1.0, v21
	v_mul_f32_e32 v20, 0xbfb8aa3b, v16
	v_mul_f32_e32 v21, 0xbfb8aa3b, v17
	v_exp_f32_e32 v20, v20
	v_exp_f32_e32 v21, v21
	v_mul_f32_e32 v22, 0xbfb8aa3b, v10
	v_mul_f32_e32 v23, 0xbfb8aa3b, v11
	v_exp_f32_e32 v22, v22
	v_exp_f32_e32 v23, v23
	v_mul_f32_e32 v24, 0xbfb8aa3b, v12
	v_mul_f32_e32 v25, 0xbfb8aa3b, v13
	v_rcp_f32_e32 v18, v18
	v_rcp_f32_e32 v19, v19
	v_add_f32_e32 v20, 1.0, v20
	v_add_f32_e32 v21, 1.0, v21
	v_exp_f32_e32 v24, v24
	v_exp_f32_e32 v25, v25
	v_rcp_f32_e32 v20, v20
	v_rcp_f32_e32 v21, v21
	v_add_f32_e32 v22, 1.0, v22
	v_add_f32_e32 v23, 1.0, v23
	v_rcp_f32_e32 v22, v22
	v_rcp_f32_e32 v23, v23
	v_add_f32_e32 v24, 1.0, v24
	v_add_f32_e32 v25, 1.0, v25
	v_pk_mul_f32 v[14:15], v[14:15], v[18:19]
	v_rcp_f32_e32 v24, v24
	v_rcp_f32_e32 v25, v25
	v_pk_mul_f32 v[6:7], v[14:15], v[6:7]
	v_pk_mul_f32 v[14:15], v[16:17], v[20:21]
	v_cvt_pk_bf16_f32 v6, v6, v7
	v_pk_mul_f32 v[8:9], v[14:15], v[8:9]
	s_nop 0
	v_cvt_pk_bf16_f32 v7, v8, v9
	v_pk_mul_f32 v[8:9], v[10:11], v[22:23]
	s_nop 0
	v_pk_mul_f32 v[2:3], v[8:9], v[2:3]
	s_nop 0
	v_cvt_pk_bf16_f32 v8, v2, v3
	v_pk_mul_f32 v[2:3], v[12:13], v[24:25]
	s_nop 0
	v_pk_mul_f32 v[2:3], v[2:3], v[4:5]
	s_nop 0
	v_cvt_pk_bf16_f32 v9, v2, v3
	v_add_co_u32_e32 v2, vcc, 0xb0000, v140
	v_mov_b32_e32 v140, v160
	s_nop 0
	v_addc_co_u32_e32 v3, vcc, 0, v141, vcc
	s_and_b64 vcc, exec, s[0:1]
	v_mov_b32_e32 v141, v161
	global_store_dwordx4 v[2:3], v[6:9], off
	s_cbranch_vccz .LBB0_1703
	s_waitcnt vmcnt(0)
	s_cmpk_gt_u32 s18, 0xff
	s_cbranch_scc1 .LBB0_1716
	s_barrier

; __device__ __forceinline__ float bflo(unsigned w) { return __uint_as_float(w << 16); }
; __device__ __forceinline__ float bfhi(unsigned w) { return __uint_as_float(w & 0xffff0000u); }
; template <bool LAST>
; __device__ __forceinline__ void phase_moe_combine(bf16_t* X1, const bf16_t* Ye, const int* INV, const float* GATE, const float* g2  , int nrows,
;                                                   const float* gain, const float* modn, bf16_t* Hb, float* out) {
;     const int lane = threadIdx.x & 63, wave = threadIdx.x >> 6;
;     const int gw = blockIdx.x * 8 + wave, NGW = gridDim.x * 8;
;     int inv = -1; u32x4 nx[4];
;     if (gw < nrows) { inv = INV[(size_t)gw * NE + (lane & 15)];
; #pragma unroll
;         for (int i = 0; i < 4; ++i) nx[i] = *(const u32x4*)(X1 + (size_t)gw * D + 8 * (lane + 64 * i)); }
;     for (int r = gw; r < nrows; r += NGW) {
;         const int mrow = r < M_LAT ? (r >> 12) : 4;
;         const int slotv = inv;
;         if (r + NGW < nrows) inv = INV[(size_t)(r + NGW) * NE + (lane & 15)];
;     ...
;         bf16_t* xr = X1 + (size_t)r * D; const float* gr = g2 + (size_t)mrow * 12288;
;         u32x4 xw_[4];
; #pragma unroll
;         for (int j = 0; j < 4; ++j) xw_[j] = nx[j];
;         if (r + NGW < nrows) {
; #pragma unroll
;             for (int j = 0; j < 4; ++j) nx[j] = *(const u32x4*)(X1 + (size_t)(r + NGW) * D + 8 * (lane + 64 * j)); }
;         f32x4 v[4][2]; float ss = 0.f;
; #pragma unroll
;         for (int j = 0; j < 4; ++j) { const int k = 8 * (lane + 64 * j); const u32x4 w = xw_[j];
;             v[j][0] = (f32x4){bflo(w.x), bfhi(w.x), bflo(w.y), bfhi(w.y)} + *(const f32x4*)(gr + k) * acc[j][0];
;             v[j][1] = (f32x4){bflo(w.z), bfhi(w.z), bflo(w.w), bfhi(w.w)} + *(const f32x4*)(gr + k + 4) * acc[j][1];
; #pragma unroll
;             for (int t2 = 0; t2 < 2; ++t2) ss += (v[j][t2][0] * v[j][t2][0] + v[j][t2][1] * v[j][t2][1]) + (v[j][t2][2] * v[j][t2][2] + v[j][t2][3] * v[j][t2][3]); }
;         const float rstd = rsqrtf(wave_sum(ss) * (1.f / D) + EPS);
;         if (LAST) {
; #pragma unroll
;             for (int j = 0; j < 4; ++j) { const int k = 8 * (lane + 64 * j);
;                 *(f32x4*)(out + (size_t)r * D + k) = v[j][0] * rstd * *(const f32x4*)(gain + k); *(f32x4*)(out + (size_t)r * D + k + 4) = v[j][1] * rstd * *(const f32x4*)(gain + k + 4); }
.LBB0_1836:
	v_readlane_b32 s2, v254, 0
	v_readlane_b32 s3, v254, 1
	s_cmp_gt_i32 s2, 21
	s_cselect_b64 s[2:3], -1, 0
	s_xor_b64 s[0:1], s[0:1], -1
	s_or_b64 s[0:1], s[2:3], s[0:1]
	s_and_b64 vcc, exec, s[0:1]
	s_cbranch_vccnz .LBB0_1852
	v_readlane_b32 s0, v255, 10
	s_movk_i32 s12, 0x4000
	v_readlane_b32 s1, v255, 11
	v_lshl_or_b32 v50, s0, 3, v228
	v_cmp_gt_i32_e32 vcc, s12, v50
	s_and_saveexec_b64 s[0:1], vcc
	s_cbranch_execz .LBB0_1852
	v_and_b32_e32 v1, 15, v0
	v_lshlrev_b32_e32 v0, 3, v0
	v_ashrrev_i32_e32 v51, 31, v50
	v_readlane_b32 s2, v255, 5
	v_and_b32_e32 v18, 0x1f8, v0
	v_mov_b32_e32 v33, 0
	v_lshlrev_b32_e32 v32, 2, v1
	v_lshlrev_b64 v[0:1], 12, v[50:51]
	v_readlane_b32 s3, v255, 6
	v_lshlrev_b32_e32 v20, 1, v18
	v_mov_b32_e32 v21, v33
	v_lshl_add_u64 v[0:1], s[2:3], 0, v[0:1]
	v_readlane_b32 s6, v255, 14
	v_lshl_add_u64 v[22:23], v[0:1], 0, v[20:21]
	v_lshlrev_b64 v[0:1], 6, v[50:51]
	v_readlane_b32 s7, v255, 15
	v_mbcnt_lo_u32_b32 v17, -1, 0
	v_mbcnt_hi_u32_b32 v17, -1, v17
	v_lshl_add_u64 v[0:1], s[6:7], 0, v[0:1]
	v_lshl_add_u64 v[24:25], v[0:1], 0, v[32:33]
	global_load_dword v16, v[24:25], off
	global_load_dwordx4 v[12:15], v[22:23], off
	global_load_dwordx4 v[8:11], v[22:23], off offset:1024
	global_load_dwordx4 v[4:7], v[22:23], off offset:2048
	global_load_dwordx4 v[0:3], v[22:23], off offset:3072
	v_and_b32_e32 v19, 64, v17
	v_add_u32_e32 v19, 64, v19
	v_xor_b32_e32 v23, 1, v17
	v_cmp_lt_i32_e32 vcc, v23, v19
	v_or_b32_e32 v22, 0x400, v18
	v_lshlrev_b32_e32 v26, 2, v18
	v_cndmask_b32_e32 v23, v17, v23, vcc
	v_lshlrev_b32_e32 v86, 2, v23
	v_xor_b32_e32 v23, 2, v17
	v_cmp_lt_i32_e32 vcc, v23, v19
	v_mov_b32_e32 v27, v33
	v_or_b32_e32 v24, 0x600, v18
	v_cndmask_b32_e32 v23, v17, v23, vcc
	v_lshlrev_b32_e32 v87, 2, v23
	v_xor_b32_e32 v23, 4, v17
	v_cmp_lt_i32_e32 vcc, v23, v19
	v_lshl_add_u64 v[38:39], s[36:37], 0, v[26:27]
	v_lshlrev_b32_e32 v26, 2, v22
	v_cndmask_b32_e32 v23, v17, v23, vcc
	v_lshlrev_b32_e32 v88, 2, v23
	v_xor_b32_e32 v23, 8, v17
	v_cmp_lt_i32_e32 vcc, v23, v19
	s_add_u32 s4, s94, 0x146000
	v_readlane_b32 s0, v255, 9
	v_cndmask_b32_e32 v23, v17, v23, vcc
	v_lshlrev_b32_e32 v89, 2, v23
	v_xor_b32_e32 v23, 16, v17
	v_cmp_lt_i32_e32 vcc, v23, v19
	v_lshl_add_u64 v[40:41], s[36:37], 0, v[26:27]
	v_lshlrev_b32_e32 v26, 2, v24
	v_cndmask_b32_e32 v23, v17, v23, vcc
	v_lshlrev_b32_e32 v90, 2, v23
	v_xor_b32_e32 v23, 32, v17
	v_cmp_lt_i32_e32 vcc, v23, v19
	s_addc_u32 s5, s95, 0
	s_lshl_b32 s13, s0, 3
	v_cndmask_b32_e32 v17, v17, v23, vcc
	v_lshl_add_u64 v[34:35], s[6:7], 0, v[32:33]
	v_lshl_add_u64 v[36:37], s[78:79], 0, v[20:21]
	v_lshl_add_u64 v[42:43], s[36:37], 0, v[26:27]
	v_lshlrev_b32_e32 v91, 2, v17
	v_lshl_add_u64 v[44:45], s[2:3], 0, v[20:21]
	s_mov_b64 s[6:7], 0
	s_movk_i32 s14, 0x3fff
	v_lshlrev_b32_e32 v32, 2, v18
	v_lshlrev_b32_e32 v46, 2, v22
	v_lshlrev_b32_e32 v48, 2, v24
	v_mov_b32_e32 v92, 0x358637bd
	s_mov_b32 s15, 0x800000
	global_load_dwordx4 v[170:173], v[38:39], off
	global_load_dwordx4 v[174:177], v[38:39], off offset:16
	global_load_dwordx4 v[178:181], v[38:39], off offset:2048
	global_load_dwordx4 v[182:185], v[38:39], off offset:2064
	global_load_dwordx4 v[186:189], v[40:41], off
	global_load_dwordx4 v[190:193], v[40:41], off offset:16
	global_load_dwordx4 v[194:197], v[42:43], off
	global_load_dwordx4 v[198:201], v[42:43], off offset:16
	s_waitcnt vmcnt(0)
	v_mov_b32_e32 v93, v16
	s_branch .LBB0_1840
.LBB0_1839:
	s_or_b64 exec, exec, s[2:3]
	v_ashrrev_i32_e32 v47, 12, v50
	v_mul_hi_i32_i24_e32 v95, 0xc000, v47
	v_mul_i32_i24_e32 v94, 0xc000, v47
	v_lshl_add_u64 v[118:119], s[4:5], 0, v[94:95]
	v_mov_b32_e32 v47, v33
	v_lshl_add_u64 v[110:111], v[118:119], 0, v[32:33]
	v_lshl_add_u64 v[120:121], v[118:119], 0, v[46:47]
	global_load_dwordx4 v[94:97], v[110:111], off
	global_load_dwordx4 v[98:101], v[110:111], off offset:16
	global_load_dwordx4 v[102:105], v[110:111], off offset:2048
	global_load_dwordx4 v[106:109], v[110:111], off offset:2064
	s_nop 0
	global_load_dwordx4 v[110:113], v[120:121], off
	global_load_dwordx4 v[114:117], v[120:121], off offset:16
	v_mov_b32_e32 v49, v33
	v_lshl_add_u64 v[128:129], v[118:119], 0, v[48:49]
	global_load_dwordx4 v[118:121], v[128:129], off offset:16
	global_load_dwordx4 v[122:125], v[128:129], off
	v_lshlrev_b32_e32 v126, 16, v12
	v_and_b32_e32 v127, 0xffff0000, v12
	v_lshlrev_b32_e32 v12, 16, v13
	v_and_b32_e32 v13, 0xffff0000, v13
	v_lshlrev_b32_e32 v128, 16, v14
	v_and_b32_e32 v129, 0xffff0000, v14
	v_lshlrev_b32_e32 v14, 16, v15
	v_and_b32_e32 v15, 0xffff0000, v15
	v_lshlrev_b32_e32 v130, 16, v8
	v_and_b32_e32 v131, 0xffff0000, v8
	v_lshlrev_b32_e32 v8, 16, v9
	v_and_b32_e32 v9, 0xffff0000, v9
	v_lshlrev_b32_e32 v136, 16, v6
	v_and_b32_e32 v137, 0xffff0000, v6
	v_lshlrev_b32_e32 v6, 16, v7
	v_and_b32_e32 v7, 0xffff0000, v7
	v_lshlrev_b32_e32 v132, 16, v10
	v_and_b32_e32 v133, 0xffff0000, v10
	v_lshlrev_b32_e32 v10, 16, v11
	v_and_b32_e32 v11, 0xffff0000, v11
	v_lshlrev_b32_e32 v134, 16, v4
	v_and_b32_e32 v135, 0xffff0000, v4
	v_lshlrev_b32_e32 v4, 16, v5
	v_and_b32_e32 v5, 0xffff0000, v5
	s_waitcnt vmcnt(0)
; __device__ __forceinline__ float bflo(unsigned w) { return __uint_as_float(w << 16); }
; __device__ __forceinline__ float bfhi(unsigned w) { return __uint_as_float(w & 0xffff0000u); }
; template <bool LAST>
; __device__ __forceinline__ void phase_moe_combine(bf16_t* X1, const bf16_t* Ye, const int* INV, const float* GATE, const float* g2  , int nrows,
;                                                   const float* gain, const float* modn, bf16_t* Hb, float* out) {
;     ...
;         f32x4 v[4][2]; float ss = 0.f;
; #pragma unroll
;         for (int j = 0; j < 4; ++j) { const int k = 8 * (lane + 64 * j); const u32x4 w = xw_[j];
;             v[j][0] = (f32x4){bflo(w.x), bfhi(w.x), bflo(w.y), bfhi(w.y)} + *(const f32x4*)(gr + k) * acc[j][0];
;             v[j][1] = (f32x4){bflo(w.z), bfhi(w.z), bflo(w.w), bfhi(w.w)} + *(const f32x4*)(gr + k + 4) * acc[j][1];
; #pragma unroll
;             for (int t2 = 0; t2 < 2; ++t2) ss += (v[j][t2][0] * v[j][t2][0] + v[j][t2][1] * v[j][t2][1]) + (v[j][t2][2] * v[j][t2][2] + v[j][t2][3] * v[j][t2][3]); }
;         const float rstd = rsqrtf(wave_sum(ss) * (1.f / D) + EPS);
;         if (LAST) {
; #pragma unroll
;             for (int j = 0; j < 4; ++j) { const int k = 8 * (lane + 64 * j);
;                 *(f32x4*)(out + (size_t)r * D + k) = v[j][0] * rstd * *(const f32x4*)(gain + k); *(f32x4*)(out + (size_t)r * D + k + 4) = v[j][1] * rstd * *(const f32x4*)(gain + k + 4); }
	v_pk_fma_f32 v[12:13], v[82:83], v[96:97], v[12:13]
	v_pk_fma_f32 v[82:83], v[84:85], v[94:95], v[126:127]
	v_pk_fma_f32 v[14:15], v[78:79], v[100:101], v[14:15]
	v_pk_fma_f32 v[78:79], v[80:81], v[98:99], v[128:129]
	v_pk_fma_f32 v[8:9], v[72:73], v[104:105], v[8:9]
	v_pk_fma_f32 v[72:73], v[76:77], v[102:103], v[130:131]
	v_pk_fma_f32 v[62:63], v[62:63], v[116:117], v[6:7]
	v_mov_b32_e32 v6, v83
	v_mov_b32_e32 v7, v79
	v_mov_b32_e32 v76, v13
	v_mov_b32_e32 v77, v15
	v_pk_fma_f32 v[10:11], v[68:69], v[108:109], v[10:11]
	v_pk_fma_f32 v[68:69], v[74:75], v[106:107], v[132:133]
	v_pk_fma_f32 v[64:65], v[64:65], v[112:113], v[4:5]
	v_mov_b32_e32 v4, v82
	v_mov_b32_e32 v5, v78
	v_mov_b32_e32 v74, v12
	v_mov_b32_e32 v75, v14
	v_pk_mul_f32 v[80:81], v[72:73], v[72:73]
	v_pk_mul_f32 v[84:85], v[8:9], v[8:9]
	v_pk_mul_f32 v[6:7], v[6:7], v[6:7]
	v_pk_mul_f32 v[76:77], v[76:77], v[76:77]
	v_pk_mov_b32 v[102:103], v[80:81], v[84:85] op_sel:[1,0]
	v_mov_b32_e32 v81, v85
	v_pk_fma_f32 v[4:5], v[4:5], v[4:5], v[6:7]
	v_pk_fma_f32 v[6:7], v[74:75], v[74:75], v[76:77]
	v_pk_fma_f32 v[70:71], v[70:71], v[110:111], v[134:135]
	v_mul_f32_e32 v94, v69, v69
	v_mul_f32_e32 v96, v11, v11
	v_pk_add_f32 v[74:75], v[102:103], v[80:81]
	v_pk_add_f32 v[4:5], v[4:5], v[6:7]
	v_mul_f32_e32 v51, v70, v70
	v_mul_f32_e32 v53, v71, v71
	v_mul_f32_e32 v104, v64, v64
	v_mul_f32_e32 v105, v65, v65
	v_pk_fma_f32 v[84:85], v[68:69], v[68:69], v[94:95] op_sel_hi:[1,1,0]
	v_pk_fma_f32 v[94:95], v[10:11], v[10:11], v[96:97] op_sel_hi:[1,1,0]
	v_pk_add_f32 v[6:7], v[74:75], v[74:75] op_sel:[0,1] op_sel_hi:[1,0]
	v_pk_add_f32 v[4:5], v[4:5], v[4:5] op_sel:[0,1] op_sel_hi:[1,0]
	v_mov_b32_e32 v85, v104
	v_mov_b32_e32 v95, v105
	v_mov_b32_e32 v7, v53
	v_mov_b32_e32 v5, v51
	v_pk_add_f32 v[74:75], v[84:85], v[94:95]
	v_pk_add_f32 v[4:5], v[4:5], v[6:7]
	v_pk_fma_f32 v[66:67], v[66:67], v[114:115], v[136:137]
	v_pk_add_f32 v[74:75], v[4:5], v[74:75]
	s_nop 0
	v_lshlrev_b32_e32 v80, 16, v0
	v_and_b32_e32 v81, 0xffff0000, v0
	v_lshlrev_b32_e32 v0, 16, v1
	v_and_b32_e32 v1, 0xffff0000, v1
	v_pk_mul_f32 v[98:99], v[66:67], v[66:67]
	v_pk_mul_f32 v[100:101], v[62:63], v[62:63]
	v_pk_fma_f32 v[58:59], v[58:59], v[124:125], v[0:1]
	v_lshlrev_b32_e32 v0, 16, v2
	v_and_b32_e32 v1, 0xffff0000, v2
	v_pk_mov_b32 v[96:97], v[98:99], v[100:101] op_sel:[1,0]
	v_mov_b32_e32 v99, v101
	v_lshlrev_b32_e32 v2, 16, v3
	v_and_b32_e32 v3, 0xffff0000, v3
	v_pk_fma_f32 v[84:85], v[56:57], v[118:119], v[0:1]
	v_pk_add_f32 v[76:77], v[96:97], v[98:99]
	v_pk_fma_f32 v[60:61], v[60:61], v[122:123], v[80:81]
	v_pk_fma_f32 v[80:81], v[54:55], v[120:121], v[2:3]
	v_mul_f32_e32 v2, v84, v84
	v_pk_add_f32 v[0:1], v[74:75], v[74:75] op_sel:[0,1] op_sel_hi:[1,0]
	v_mul_f32_e32 v51, v85, v85
	v_mov_b32_e32 v1, v2
	v_pk_add_f32 v[2:3], v[76:77], v[76:77] op_sel:[0,1] op_sel_hi:[1,0]
	v_mul_f32_e32 v54, v59, v59
	v_mov_b32_e32 v3, v51
	v_pk_add_f32 v[0:1], v[0:1], v[2:3]
	v_mul_f32_e32 v2, v61, v61
	v_mul_f32_e32 v53, v80, v80
	v_mul_f32_e32 v56, v81, v81
	v_pk_fma_f32 v[2:3], v[60:61], v[60:61], v[2:3] op_sel_hi:[1,1,0]
	v_pk_fma_f32 v[54:55], v[58:59], v[58:59], v[54:55] op_sel_hi:[1,1,0]
	v_mov_b32_e32 v3, v53
	v_mov_b32_e32 v55, v56
	v_pk_add_f32 v[2:3], v[2:3], v[54:55]
	v_ashrrev_i32_e32 v51, 31, v50
	v_pk_add_f32 v[0:1], v[0:1], v[2:3]
	s_nop 0
	v_add_f32_e32 v0, v0, v1
	ds_bpermute_b32 v1, v86, v0
	s_waitcnt lgkmcnt(0)
	v_add_f32_e32 v0, v0, v1
	ds_bpermute_b32 v1, v87, v0
	s_waitcnt lgkmcnt(0)
	v_add_f32_e32 v0, v0, v1
	ds_bpermute_b32 v1, v88, v0
	s_waitcnt lgkmcnt(0)
	v_add_f32_e32 v0, v0, v1
	ds_bpermute_b32 v1, v89, v0
	s_waitcnt lgkmcnt(0)
	v_add_f32_e32 v0, v0, v1
	ds_bpermute_b32 v1, v90, v0
	s_waitcnt lgkmcnt(0)
	v_add_f32_e32 v0, v0, v1
	ds_bpermute_b32 v1, v91, v0
	s_waitcnt lgkmcnt(0)
	v_add_f32_e32 v0, v0, v1
	v_fmamk_f32 v0, v0, 0x3a000000, v92
	v_mul_f32_e32 v1, 0x4b800000, v0
	v_cmp_gt_f32_e32 vcc, s15, v0
	s_nop 1
	v_cndmask_b32_e32 v0, v0, v1, vcc
	v_rsq_f32_e32 v0, v0
	s_nop 0
	v_mul_f32_e32 v1, 0x45800000, v0
	v_cndmask_b32_e32 v74, v0, v1, vcc
	v_lshlrev_b64 v[0:1], 13, v[50:51]
	v_lshl_add_u64 v[50:51], s[92:93], 0, v[0:1]
	v_pk_mul_f32 v[0:1], v[82:83], v[74:75] op_sel_hi:[1,0]
	v_pk_mul_f32 v[2:3], v[12:13], v[74:75] op_sel_hi:[1,0]
	s_nop 0
	v_pk_mul_f32 v[0:1], v[170:171], v[0:1]
	v_pk_mul_f32 v[2:3], v[172:173], v[2:3]
	v_lshl_add_u64 v[4:5], v[50:51], 0, v[32:33]
	global_store_dwordx4 v[4:5], v[0:3], off
	s_nop 0
	v_pk_mul_f32 v[6:7], v[14:15], v[74:75] op_sel_hi:[1,0]
	v_pk_mul_f32 v[12:13], v[78:79], v[74:75] op_sel_hi:[1,0]
	s_nop 0
	v_pk_mul_f32 v[2:3], v[176:177], v[6:7]
	v_pk_mul_f32 v[0:1], v[174:175], v[12:13]
	global_store_dwordx4 v[4:5], v[0:3], off offset:16
	s_nop 0
	v_pk_mul_f32 v[6:7], v[8:9], v[74:75] op_sel_hi:[1,0]
	v_pk_mul_f32 v[8:9], v[72:73], v[74:75] op_sel_hi:[1,0]
	v_mov_b64_e32 v[12:13], v[16:17]
	v_mov_b64_e32 v[14:15], v[18:19]
	v_pk_mul_f32 v[18:19], v[84:85], v[74:75] op_sel_hi:[1,0]
	v_mov_b32_e32 v16, v93
	s_nop 0
	v_pk_mul_f32 v[0:1], v[178:179], v[8:9]
	v_pk_mul_f32 v[2:3], v[180:181], v[6:7]
	global_store_dwordx4 v[4:5], v[0:3], off offset:2048
	s_nop 0
	v_pk_mul_f32 v[6:7], v[10:11], v[74:75] op_sel_hi:[1,0]
	v_pk_mul_f32 v[8:9], v[68:69], v[74:75] op_sel_hi:[1,0]
	s_nop 0
	v_pk_mul_f32 v[2:3], v[184:185], v[6:7]
	v_pk_mul_f32 v[0:1], v[182:183], v[8:9]
	global_store_dwordx4 v[4:5], v[0:3], off offset:2064
	s_nop 0
	v_pk_mul_f32 v[6:7], v[64:65], v[74:75] op_sel_hi:[1,0]
	v_pk_mul_f32 v[8:9], v[70:71], v[74:75] op_sel_hi:[1,0]
	v_lshl_add_u64 v[4:5], v[50:51], 0, v[46:47]
	v_lshl_add_u64 v[50:51], v[50:51], 0, v[48:49]
	s_nop 0
	v_pk_mul_f32 v[0:1], v[186:187], v[8:9]
	v_pk_mul_f32 v[2:3], v[188:189], v[6:7]
	global_store_dwordx4 v[4:5], v[0:3], off
	s_nop 0
	v_pk_mul_f32 v[6:7], v[62:63], v[74:75] op_sel_hi:[1,0]
	v_pk_mul_f32 v[8:9], v[66:67], v[74:75] op_sel_hi:[1,0]
	s_nop 0
	v_pk_mul_f32 v[2:3], v[192:193], v[6:7]
	v_pk_mul_f32 v[0:1], v[190:191], v[8:9]
	global_store_dwordx4 v[4:5], v[0:3], off offset:16
	s_nop 0
	v_pk_mul_f32 v[4:5], v[58:59], v[74:75] op_sel_hi:[1,0]
	v_pk_mul_f32 v[6:7], v[60:61], v[74:75] op_sel_hi:[1,0]
	v_mov_b64_e32 v[8:9], v[20:21]
	v_mov_b64_e32 v[10:11], v[22:23]
	v_pk_mul_f32 v[20:21], v[80:81], v[74:75] op_sel_hi:[1,0]
	s_nop 0
	v_pk_mul_f32 v[0:1], v[194:195], v[6:7]
	v_pk_mul_f32 v[2:3], v[196:197], v[4:5]
	global_store_dwordx4 v[50:51], v[0:3], off
	s_nop 0
	v_mov_b64_e32 v[4:5], v[24:25]
	v_mov_b64_e32 v[0:1], v[28:29]
	v_mov_b64_e32 v[6:7], v[26:27]
	v_mov_b64_e32 v[2:3], v[30:31]
	s_nop 0
	v_pk_mul_f32 v[18:19], v[198:199], v[18:19]
	v_pk_mul_f32 v[20:21], v[200:201], v[20:21]
	global_store_dwordx4 v[50:51], v[18:21], off offset:16
	v_mov_b32_e32 v50, v52
	s_andn2_b64 exec, exec, s[6:7]
	s_cbranch_execz .LBB0_1852
